# selected branch: per-iteration block-bitmap read hoisted ahead of the tile barrier (shorter barrier-to-branch chain), on top of the layer-1 w_down deferral
# speedup vs baseline: 1.0062x; 1.0011x over previous
; template <int MODE> ...
;     ...
;         const int j = jlo + t; const int buf = stg;
;         if (t + 1 < NT) asm volatile("s_waitcnt vmcnt(4)" ::: "memory"); else asm volatile("s_waitcnt vmcnt(0)" ::: "memory");
;         __builtin_amdgcn_s_barrier(); asm volatile("" ::: "memory");
;         if (t + 2 < NT) { const int s2 = stg == 0 ? 2 : stg - 1; AT_ISSUE(j + 2, s2); }
;         bool rowsel = true;
;         if (MODE == 1) rowsel = ((bmrow[j >> 5] >> (j & 31)) & 1u) != 0u;
;         if (MODE != 1 || __any(rowsel)) {
.LBB0_844:
	s_lshr_b32 s98, s16, 3
	s_and_b32 s98, s98, 0x1ffffffc
	v_add_u32_e32 v202, s98, v191
	ds_read_b32 v202, v202
	s_andn2_b64 vcc, exec, s[0:1]
	s_cbranch_vccnz .LBB0_846
	s_waitcnt vmcnt(4)

; #define LAS __attribute__((address_space(3)))
; __device__ __forceinline__ void at_qkt(f32x16& p0, f32x16& p1, const LAS unsigned char* Kt, int l32, int hi, const bf16x8 (&qr)[8], const f32x16& cinit) {
;     const LAS unsigned char* kb[4];
; #pragma unroll
;     for (int dd = 0; dd < 4; ++dd) kb[dd] = Kt + KSWZ(l32, (dd * 16 + hi * 8) * 2);
; #pragma unroll
;     for (int d0 = 0; d0 < 8; ++d0) { const LAS unsigned char* a = kb[d0 & 3] + (d0 >> 2) * 128;
;         const bf16x8 b0 = *(const LAS bf16x8*)a, b1 = *(const LAS bf16x8*)(a + 32 * 256);
;         if (d0 == 0) { p0 = __builtin_amdgcn_mfma_f32_32x32x16_bf16(b0, qr[0], cinit, 0, 0, 0); p1 = __builtin_amdgcn_mfma_f32_32x32x16_bf16(b1, qr[0], cinit, 0, 0, 0); }
;         else { p0 = __builtin_amdgcn_mfma_f32_32x32x16_bf16(b0, qr[d0], p0, 0, 0, 0); p1 = __builtin_amdgcn_mfma_f32_32x32x16_bf16(b1, qr[d0], p1, 0, 0, 0); } }
; }
; template <int MODE> ...
;     ...
;         if (MODE == 1) rowsel = ((bmrow[j >> 5] >> (j & 31)) & 1u) != 0u;
;         if (MODE != 1 || __any(rowsel)) {
;         f32x16 p0, p1;
;         at_qkt(p0, p1, K_lds + buf * 16384, l32, hi, qr, negm);
;         const bool need_mask = MODE == 0 ? (64 * j + 63 > lim_min) : (MODE == 1 ? (64 * j + 63 > tq_min) : (64 * j + 63 > tq_min || 64 * j <= tq_min + 7 - WIN));
;         if (need_mask) at_mask<MODE>(p0, p1, 64 * j, hi, tq, lim, true);
;         bf16x8 pa0, pa1, pa2, pa3;
;         const float alpha = at_softmax(p0, p1, m_reg, negm, l_reg, pa0, pa1, pa2, pa3, rowsel, MODE == 1);
;         if (__any(alpha < 1.f)) { if (hi == 0) wsl[l32] = alpha; asm volatile("s_waitcnt lgkmcnt(0)" ::: "memory");
.LBB0_848:
	s_and_b32 s0, s16, 31
	s_waitcnt lgkmcnt(0)
	v_lshrrev_b32_e32 v4, s16, v202
	v_bfe_u32 v2, v202, s0, 1
	v_and_b32_e32 v4, 1, v4
	v_cmp_ne_u32_e32 vcc, 0, v2
	v_cmp_eq_u32_e64 s[6:7], 1, v4
	s_cbranch_vccz .LBB0_859
	s_lshl_b32 s17, s14, 14
	v_add_u32_e32 v2, s17, v193
	v_add_u32_e32 v8, v2, v194
	v_add_u32_e32 v9, v2, v195
	v_add_u32_e32 v10, v2, v196
	v_add_u32_e32 v2, v2, v197
	ds_read_b128 v[4:7], v8
	ds_read_b128 v[202:205], v8 offset:8192
	ds_read_b128 v[206:209], v9
	ds_read_b128 v[210:213], v9 offset:8192
	ds_read_b128 v[232:235], v10
	ds_read_b128 v[236:239], v10 offset:8192
	ds_read_b128 v[240:243], v2
	ds_read_b128 v[244:247], v2 offset:8192
	s_cmp_le_i32 s15, s11
	s_waitcnt lgkmcnt(7)
	v_mfma_f32_32x32x16_bf16 v[114:129], v[4:7], v[130:133], v[82:97]
	ds_read_b128 v[4:7], v8 offset:128
	s_waitcnt lgkmcnt(7)
	v_mfma_f32_32x32x16_bf16 v[98:113], v[202:205], v[130:133], v[82:97]
	ds_read_b128 v[202:205], v8 offset:8320
	s_waitcnt lgkmcnt(7)
	v_mfma_f32_32x32x16_bf16 v[114:129], v[206:209], v[134:137], v[114:129]
	ds_read_b128 v[206:209], v9 offset:128
	s_waitcnt lgkmcnt(7)
	v_mfma_f32_32x32x16_bf16 v[98:113], v[210:213], v[134:137], v[98:113]
	ds_read_b128 v[210:213], v9 offset:8320
	s_waitcnt lgkmcnt(7)
	v_mfma_f32_32x32x16_bf16 v[114:129], v[232:235], v[138:141], v[114:129]
	ds_read_b128 v[232:235], v10 offset:128
	s_waitcnt lgkmcnt(7)
	v_mfma_f32_32x32x16_bf16 v[98:113], v[236:239], v[138:141], v[98:113]
	ds_read_b128 v[236:239], v10 offset:8320
	s_waitcnt lgkmcnt(7)
	v_mfma_f32_32x32x16_bf16 v[114:129], v[240:243], v[142:145], v[114:129]
	ds_read_b128 v[240:243], v2 offset:128
	s_waitcnt lgkmcnt(7)
	v_mfma_f32_32x32x16_bf16 v[98:113], v[244:247], v[142:145], v[98:113]
	ds_read_b128 v[244:247], v2 offset:8320
	s_waitcnt lgkmcnt(7)
	v_mfma_f32_32x32x16_bf16 v[114:129], v[4:7], v[146:149], v[114:129]
	s_waitcnt lgkmcnt(6)
	v_mfma_f32_32x32x16_bf16 v[98:113], v[202:205], v[146:149], v[98:113]
	s_waitcnt lgkmcnt(5)
	v_mfma_f32_32x32x16_bf16 v[114:129], v[206:209], v[150:153], v[114:129]
	s_waitcnt lgkmcnt(4)
	v_mfma_f32_32x32x16_bf16 v[98:113], v[210:213], v[150:153], v[98:113]
	s_waitcnt lgkmcnt(3)
	v_mfma_f32_32x32x16_bf16 v[114:129], v[232:235], v[154:157], v[114:129]
	s_waitcnt lgkmcnt(2)
	v_mfma_f32_32x32x16_bf16 v[98:113], v[236:239], v[154:157], v[98:113]
	s_waitcnt lgkmcnt(1)
	v_mfma_f32_32x32x16_bf16 v[114:129], v[240:243], v[158:161], v[114:129]
	s_waitcnt lgkmcnt(0)
	v_mfma_f32_32x32x16_bf16 v[98:113], v[244:247], v[158:161], v[98:113]
	s_cbranch_scc1 .LBB0_851
	v_add_u32_e32 v2, s15, v198
	v_subrev_u32_e32 v5, 31, v2
	v_subrev_u32_e32 v4, 63, v2
	v_cmp_le_i32_e32 vcc, v5, v187
	v_subrev_u32_e32 v5, 30, v2
	s_nop 5
	v_cndmask_b32_e32 v98, v226, v98, vcc
	v_cmp_lt_i32_e32 vcc, v4, v187
	s_nop 1
	v_cndmask_b32_e32 v115, v226, v115, vcc
	v_cmp_le_i32_e32 vcc, v4, v187
	v_subrev_u32_e32 v4, 61, v2
	s_nop 0
	v_cndmask_b32_e32 v114, v226, v114, vcc
	v_cmp_le_i32_e32 vcc, v5, v187
	v_subrev_u32_e32 v5, 29, v2
	s_nop 0
	v_cndmask_b32_e32 v99, v226, v99, vcc
	v_cmp_le_i32_e32 vcc, v4, v187
	v_subrev_u32_e32 v4, 60, v2
	s_nop 0
	v_cndmask_b32_e32 v116, v226, v116, vcc
	v_cmp_le_i32_e32 vcc, v5, v187
	v_subrev_u32_e32 v5, 28, v2
	s_nop 0
	v_cndmask_b32_e32 v100, v226, v100, vcc
	v_cmp_le_i32_e32 vcc, v4, v187
	v_subrev_u32_e32 v4, 55, v2
	s_nop 0
	v_cndmask_b32_e32 v117, v226, v117, vcc
	v_cmp_le_i32_e32 vcc, v5, v187
	v_subrev_u32_e32 v5, 23, v2
	s_nop 0
	v_cndmask_b32_e32 v101, v226, v101, vcc
	v_cmp_le_i32_e32 vcc, v4, v187
	v_subrev_u32_e32 v4, 54, v2
	s_nop 0
	v_cndmask_b32_e32 v118, v226, v118, vcc
	v_cmp_le_i32_e32 vcc, v5, v187
	v_subrev_u32_e32 v5, 22, v2
	s_nop 0
	v_cndmask_b32_e32 v102, v226, v102, vcc
	v_cmp_le_i32_e32 vcc, v4, v187
	v_subrev_u32_e32 v4, 53, v2
	s_nop 0
	v_cndmask_b32_e32 v119, v226, v119, vcc
	v_cmp_le_i32_e32 vcc, v5, v187
	v_subrev_u32_e32 v5, 21, v2
	s_nop 0
	v_cndmask_b32_e32 v103, v226, v103, vcc
	v_cmp_le_i32_e32 vcc, v4, v187
	v_subrev_u32_e32 v4, 52, v2
	s_nop 0
	v_cndmask_b32_e32 v120, v226, v120, vcc
	v_cmp_le_i32_e32 vcc, v5, v187
	v_subrev_u32_e32 v5, 20, v2
	s_nop 0
	v_cndmask_b32_e32 v104, v226, v104, vcc
	v_cmp_le_i32_e32 vcc, v4, v187
	v_subrev_u32_e32 v4, 47, v2
	s_nop 0
	v_cndmask_b32_e32 v121, v226, v121, vcc
	v_cmp_le_i32_e32 vcc, v5, v187
	v_add_u32_e32 v5, -15, v2
	s_nop 0
	v_cndmask_b32_e32 v105, v226, v105, vcc
	v_cmp_le_i32_e32 vcc, v4, v187
	v_subrev_u32_e32 v4, 46, v2
	s_nop 0
	v_cndmask_b32_e32 v122, v226, v122, vcc
	v_cmp_le_i32_e32 vcc, v5, v187
	v_add_u32_e32 v5, -14, v2
	s_nop 0
	v_cndmask_b32_e32 v106, v226, v106, vcc
	v_cmp_le_i32_e32 vcc, v4, v187
	v_subrev_u32_e32 v4, 45, v2
	s_nop 0
	v_cndmask_b32_e32 v123, v226, v123, vcc
	v_cmp_le_i32_e32 vcc, v5, v187
	v_add_u32_e32 v5, -13, v2
	s_nop 0
	v_cndmask_b32_e32 v107, v226, v107, vcc
	v_cmp_le_i32_e32 vcc, v4, v187
	v_subrev_u32_e32 v4, 44, v2
	s_nop 0
	v_cndmask_b32_e32 v124, v226, v124, vcc
	v_cmp_le_i32_e32 vcc, v5, v187
	v_add_u32_e32 v5, -12, v2
	s_nop 0
	v_cndmask_b32_e32 v108, v226, v108, vcc
	v_cmp_le_i32_e32 vcc, v4, v187
	v_subrev_u32_e32 v4, 39, v2
	s_nop 0
	v_cndmask_b32_e32 v125, v226, v125, vcc
	v_cmp_le_i32_e32 vcc, v5, v187
	v_add_u32_e32 v5, -7, v2
	s_nop 0
	v_cndmask_b32_e32 v109, v226, v109, vcc
	v_cmp_le_i32_e32 vcc, v4, v187
	v_subrev_u32_e32 v4, 38, v2
	s_nop 0
	v_cndmask_b32_e32 v126, v226, v126, vcc
	v_cmp_le_i32_e32 vcc, v5, v187
	v_add_u32_e32 v5, -6, v2
	s_nop 0
	v_cndmask_b32_e32 v110, v226, v110, vcc
	v_cmp_le_i32_e32 vcc, v4, v187
	v_subrev_u32_e32 v4, 37, v2
	s_nop 0
	v_cndmask_b32_e32 v127, v226, v127, vcc
	v_cmp_le_i32_e32 vcc, v5, v187
	v_add_u32_e32 v5, -5, v2
	s_nop 0
	v_cndmask_b32_e32 v111, v226, v111, vcc
	v_cmp_le_i32_e32 vcc, v4, v187
	v_subrev_u32_e32 v4, 36, v2
	v_add_u32_e32 v2, -4, v2
	v_cndmask_b32_e32 v128, v226, v128, vcc
	v_cmp_le_i32_e32 vcc, v5, v187
	s_nop 1
	v_cndmask_b32_e32 v112, v226, v112, vcc
	v_cmp_le_i32_e32 vcc, v4, v187
	s_nop 1
	v_cndmask_b32_e32 v129, v226, v129, vcc
	v_cmp_le_i32_e32 vcc, v2, v187
	s_nop 1
	v_cndmask_b32_e32 v113, v226, v113, vcc
